# baseline (speedup 1.0000x reference)
.LBB2_91:
	s_setprio 2
	v_add_u32_e32 v26, s52, v23
	s_mov_b32 s2, 0xc350
	v_cmp_gt_i32_e32 vcc, s2, v26
	v_mov_b32_e32 v2, 0
	v_mov_b32_e32 v28, 0
	v_ashrrev_i32_e32 v27, 31, v26
	v_mov_b32_e32 v14, 0
	v_mov_b32_e32 v3, 0
	v_mov_b32_e32 v4, 0
	v_mov_b32_e32 v5, 0
	s_and_saveexec_b64 s[0:1], vcc
	s_cbranch_execz .LBB2_93
	v_lshlrev_b64 v[2:3], 8, v[26:27]
	v_lshl_add_u64 v[2:3], s[36:37], 0, v[2:3]
	v_mov_b32_e32 v25, 0
	v_lshl_add_u64 v[6:7], v[2:3], 0, v[24:25]
	v_lshl_add_u64 v[8:9], v[26:27], 2, s[44:45]
	global_load_dwordx4 v[2:5], v[6:7], off
	global_load_dword v14, v[8:9], off

.LBB3_91:
	s_setprio 2
	v_add_u32_e32 v22, s52, v19
	s_mov_b32 s2, 0xc350
	v_cmp_gt_i32_e32 vcc, s2, v22
	v_mov_b32_e32 v2, 0
	v_mov_b32_e32 v24, 0
	v_ashrrev_i32_e32 v23, 31, v22
	v_mov_b32_e32 v14, 0
	v_mov_b32_e32 v3, 0
	v_mov_b32_e32 v4, 0
	v_mov_b32_e32 v5, 0
	s_and_saveexec_b64 s[0:1], vcc
	s_cbranch_execz .LBB3_93
	v_lshlrev_b64 v[2:3], 8, v[22:23]
	v_lshl_add_u64 v[2:3], s[36:37], 0, v[2:3]
	v_mov_b32_e32 v21, 0
	v_lshl_add_u64 v[6:7], v[2:3], 0, v[20:21]
	v_lshl_add_u64 v[8:9], v[22:23], 2, s[44:45]
	global_load_dwordx4 v[2:5], v[6:7], off
	global_load_dword v14, v[8:9], off

.LBB4_91:
	s_setprio 2
	v_add_u32_e32 v16, s50, v38
	s_mov_b32 s0, 0xc350
	v_cmp_gt_i32_e32 vcc, s0, v16
	s_mov_b32 s0, 0xc34f
	v_cmp_lt_i32_e64 s[0:1], s0, v16
	s_and_saveexec_b64 s[2:3], s[0:1]
	s_xor_b64 s[0:1], exec, s[2:3]
	v_mov_b32_e32 v17, 0
	s_or_saveexec_b64 s[0:1], s[0:1]
	v_mov_b32_e32 v2, 0
	v_mov_b32_e32 v14, 0
	v_mov_b32_e32 v3, 0
	v_mov_b32_e32 v4, 0
	v_mov_b32_e32 v5, 0
	s_xor_b64 exec, exec, s[0:1]
	s_cbranch_execz .LBB4_95
	v_ashrrev_i32_e32 v17, 31, v16
	v_lshlrev_b64 v[2:3], 8, v[16:17]
	v_lshl_add_u64 v[2:3], s[36:37], 0, v[2:3]
	v_mov_b32_e32 v19, 0
	v_lshl_add_u64 v[6:7], v[2:3], 0, v[18:19]
	v_lshl_add_u64 v[8:9], v[16:17], 2, s[44:45]
	global_load_dwordx4 v[2:5], v[6:7], off
	global_load_dword v14, v[8:9], off
